# k_l2 sort direction alternates per 1024-block generation (ascending/descending column windows) and layer-1 block order permuted so its 512-block generations alternate direction too
# speedup vs baseline: 1.0174x; 1.0174x over previous
.LBB3_46:
	s_and_b64 vcc, exec, s[0:1]
	s_cbranch_vccz .LBB3_141
	s_ashr_i32 s37, s36, 31
	s_lshl_b64 s[0:1], s[36:37], 3
	s_add_u32 s0, s2, s0
	s_addc_u32 s1, s3, s1
	s_mov_b32 s6, 0x20000
	s_add_i32 s8, s44, 31
	s_lshr_b32 s8, s8, 5
	s_add_i32 s8, s8, -1
	s_lshl_b32 s9, s42, 2
	s_sub_i32 s8, s8, s9
	s_bfe_u32 s8, s8, 0x1000a
	s_mul_i32 s8, s8, 31
	v_mov_b32_e32 v66, 0
	v_mov_b32_e32 v67, 0
	v_mov_b32_e32 v68, 0
	v_mov_b32_e32 v69, 0
	v_lshl_add_u32 v1, v0, 4, s6
	ds_write_b128 v1, v[66:69]
	v_mov_b32_e32 v79, 1
	v_add_u32_e32 v76, 0, v0
	v_cmp_gt_i32_e32 vcc, s33, v76
	v_lshlrev_b32_e32 v76, 3, v76
	s_and_saveexec_b64 s[4:5], vcc
	global_load_dwordx2 v[2:3], v76, s[0:1] nt
	s_or_b64 exec, exec, s[4:5]
	v_add_u32_e32 v76, 1024, v0
	v_cmp_gt_i32_e32 vcc, s33, v76
	v_lshlrev_b32_e32 v76, 3, v76
	s_and_saveexec_b64 s[4:5], vcc
	global_load_dwordx2 v[4:5], v76, s[0:1] nt
	s_or_b64 exec, exec, s[4:5]
	v_add_u32_e32 v76, 2048, v0
	v_cmp_gt_i32_e32 vcc, s33, v76
	v_lshlrev_b32_e32 v76, 3, v76
	s_and_saveexec_b64 s[4:5], vcc
	global_load_dwordx2 v[6:7], v76, s[0:1] nt
	s_or_b64 exec, exec, s[4:5]
	v_add_u32_e32 v76, 3072, v0
	v_cmp_gt_i32_e32 vcc, s33, v76
	v_lshlrev_b32_e32 v76, 3, v76
	s_and_saveexec_b64 s[4:5], vcc
	global_load_dwordx2 v[8:9], v76, s[0:1] nt
	s_or_b64 exec, exec, s[4:5]
	v_add_u32_e32 v76, 4096, v0
	v_cmp_gt_i32_e32 vcc, s33, v76
	v_lshlrev_b32_e32 v76, 3, v76
	s_and_saveexec_b64 s[4:5], vcc
	global_load_dwordx2 v[10:11], v76, s[0:1] nt
	s_or_b64 exec, exec, s[4:5]
	v_add_u32_e32 v76, 5120, v0
	v_cmp_gt_i32_e32 vcc, s33, v76
	v_lshlrev_b32_e32 v76, 3, v76
	s_and_saveexec_b64 s[4:5], vcc
	global_load_dwordx2 v[12:13], v76, s[0:1] nt
	s_or_b64 exec, exec, s[4:5]
	v_add_u32_e32 v76, 6144, v0
	v_cmp_gt_i32_e32 vcc, s33, v76
	v_lshlrev_b32_e32 v76, 3, v76
	s_and_saveexec_b64 s[4:5], vcc
	global_load_dwordx2 v[14:15], v76, s[0:1] nt
	s_or_b64 exec, exec, s[4:5]
	v_add_u32_e32 v76, 7168, v0
	v_cmp_gt_i32_e32 vcc, s33, v76
	v_lshlrev_b32_e32 v76, 3, v76
	s_and_saveexec_b64 s[4:5], vcc
	global_load_dwordx2 v[16:17], v76, s[0:1] nt
	s_or_b64 exec, exec, s[4:5]
	v_add_u32_e32 v76, 8192, v0
	v_cmp_gt_i32_e32 vcc, s33, v76
	v_lshlrev_b32_e32 v76, 3, v76
	s_and_saveexec_b64 s[4:5], vcc
	global_load_dwordx2 v[18:19], v76, s[0:1] nt
	s_or_b64 exec, exec, s[4:5]
	v_add_u32_e32 v76, 9216, v0
	v_cmp_gt_i32_e32 vcc, s33, v76
	v_lshlrev_b32_e32 v76, 3, v76
	s_and_saveexec_b64 s[4:5], vcc
	global_load_dwordx2 v[20:21], v76, s[0:1] nt
	s_or_b64 exec, exec, s[4:5]
	v_add_u32_e32 v76, 10240, v0
	v_cmp_gt_i32_e32 vcc, s33, v76
	v_lshlrev_b32_e32 v76, 3, v76
	s_and_saveexec_b64 s[4:5], vcc
	global_load_dwordx2 v[22:23], v76, s[0:1] nt
	s_or_b64 exec, exec, s[4:5]
	v_add_u32_e32 v76, 11264, v0
	v_cmp_gt_i32_e32 vcc, s33, v76
	v_lshlrev_b32_e32 v76, 3, v76
	s_and_saveexec_b64 s[4:5], vcc
	global_load_dwordx2 v[24:25], v76, s[0:1] nt
	s_or_b64 exec, exec, s[4:5]
	v_add_u32_e32 v76, 12288, v0
	v_cmp_gt_i32_e32 vcc, s33, v76
	v_lshlrev_b32_e32 v76, 3, v76
	s_and_saveexec_b64 s[4:5], vcc
	global_load_dwordx2 v[26:27], v76, s[0:1] nt
	s_or_b64 exec, exec, s[4:5]
	v_add_u32_e32 v76, 13312, v0
	v_cmp_gt_i32_e32 vcc, s33, v76
	v_lshlrev_b32_e32 v76, 3, v76
	s_and_saveexec_b64 s[4:5], vcc
	global_load_dwordx2 v[28:29], v76, s[0:1] nt
	s_or_b64 exec, exec, s[4:5]
	v_add_u32_e32 v76, 14336, v0
	v_cmp_gt_i32_e32 vcc, s33, v76
	v_lshlrev_b32_e32 v76, 3, v76
	s_and_saveexec_b64 s[4:5], vcc
	global_load_dwordx2 v[30:31], v76, s[0:1] nt
	s_or_b64 exec, exec, s[4:5]
	v_add_u32_e32 v76, 15360, v0
	v_cmp_gt_i32_e32 vcc, s33, v76
	v_lshlrev_b32_e32 v76, 3, v76
	s_and_saveexec_b64 s[4:5], vcc
	global_load_dwordx2 v[32:33], v76, s[0:1] nt
	s_or_b64 exec, exec, s[4:5]
	s_waitcnt lgkmcnt(0)
	s_barrier
	s_waitcnt vmcnt(15)
	v_add_u32_e32 v76, 0, v0
	v_cmp_gt_i32_e32 vcc, s33, v76
	v_lshrrev_b32_e32 v76, 25, v2
	v_bfe_u32 v77, v2, 13, 12
	v_min_u32_e32 v77, 31, v77
	v_xor_b32_e32 v77, s8, v77
	v_lshl_or_b32 v76, v76, 5, v77
	v_lshl_add_u32 v50, v76, 2, s6
	s_and_saveexec_b64 s[4:5], vcc
	ds_add_rtn_u32 v34, v50, v79
	s_or_b64 exec, exec, s[4:5]
	s_waitcnt vmcnt(14)
	v_add_u32_e32 v76, 1024, v0
	v_cmp_gt_i32_e32 vcc, s33, v76
	v_lshrrev_b32_e32 v76, 25, v4
	v_bfe_u32 v77, v4, 13, 12
	v_min_u32_e32 v77, 31, v77
	v_xor_b32_e32 v77, s8, v77
	v_lshl_or_b32 v76, v76, 5, v77
	v_lshl_add_u32 v51, v76, 2, s6
	s_and_saveexec_b64 s[4:5], vcc
	ds_add_rtn_u32 v35, v51, v79
	s_or_b64 exec, exec, s[4:5]
	s_waitcnt vmcnt(13)
	v_add_u32_e32 v76, 2048, v0
	v_cmp_gt_i32_e32 vcc, s33, v76
	v_lshrrev_b32_e32 v76, 25, v6
	v_bfe_u32 v77, v6, 13, 12
	v_min_u32_e32 v77, 31, v77
	v_xor_b32_e32 v77, s8, v77
	v_lshl_or_b32 v76, v76, 5, v77
	v_lshl_add_u32 v52, v76, 2, s6
	s_and_saveexec_b64 s[4:5], vcc
	ds_add_rtn_u32 v36, v52, v79
	s_or_b64 exec, exec, s[4:5]
	s_waitcnt vmcnt(12)
	v_add_u32_e32 v76, 3072, v0
	v_cmp_gt_i32_e32 vcc, s33, v76
	v_lshrrev_b32_e32 v76, 25, v8
	v_bfe_u32 v77, v8, 13, 12
	v_min_u32_e32 v77, 31, v77
	v_xor_b32_e32 v77, s8, v77
	v_lshl_or_b32 v76, v76, 5, v77
	v_lshl_add_u32 v53, v76, 2, s6
	s_and_saveexec_b64 s[4:5], vcc
	ds_add_rtn_u32 v37, v53, v79
	s_or_b64 exec, exec, s[4:5]
	s_waitcnt vmcnt(11)
	v_add_u32_e32 v76, 4096, v0
	v_cmp_gt_i32_e32 vcc, s33, v76
	v_lshrrev_b32_e32 v76, 25, v10
	v_bfe_u32 v77, v10, 13, 12
	v_min_u32_e32 v77, 31, v77
	v_xor_b32_e32 v77, s8, v77
	v_lshl_or_b32 v76, v76, 5, v77
	v_lshl_add_u32 v54, v76, 2, s6
	s_and_saveexec_b64 s[4:5], vcc
	ds_add_rtn_u32 v38, v54, v79
	s_or_b64 exec, exec, s[4:5]
	s_waitcnt vmcnt(10)
	v_add_u32_e32 v76, 5120, v0
	v_cmp_gt_i32_e32 vcc, s33, v76
	v_lshrrev_b32_e32 v76, 25, v12
	v_bfe_u32 v77, v12, 13, 12
	v_min_u32_e32 v77, 31, v77
	v_xor_b32_e32 v77, s8, v77
	v_lshl_or_b32 v76, v76, 5, v77
	v_lshl_add_u32 v55, v76, 2, s6
	s_and_saveexec_b64 s[4:5], vcc
	ds_add_rtn_u32 v39, v55, v79
	s_or_b64 exec, exec, s[4:5]
	s_waitcnt vmcnt(9)
	v_add_u32_e32 v76, 6144, v0
	v_cmp_gt_i32_e32 vcc, s33, v76
	v_lshrrev_b32_e32 v76, 25, v14
	v_bfe_u32 v77, v14, 13, 12
	v_min_u32_e32 v77, 31, v77
	v_xor_b32_e32 v77, s8, v77
	v_lshl_or_b32 v76, v76, 5, v77
	v_lshl_add_u32 v56, v76, 2, s6
	s_and_saveexec_b64 s[4:5], vcc
	ds_add_rtn_u32 v40, v56, v79
	s_or_b64 exec, exec, s[4:5]
	s_waitcnt vmcnt(8)
	v_add_u32_e32 v76, 7168, v0
	v_cmp_gt_i32_e32 vcc, s33, v76
	v_lshrrev_b32_e32 v76, 25, v16
	v_bfe_u32 v77, v16, 13, 12
	v_min_u32_e32 v77, 31, v77
	v_xor_b32_e32 v77, s8, v77
	v_lshl_or_b32 v76, v76, 5, v77
	v_lshl_add_u32 v57, v76, 2, s6
	s_and_saveexec_b64 s[4:5], vcc
	ds_add_rtn_u32 v41, v57, v79
	s_or_b64 exec, exec, s[4:5]
	s_waitcnt vmcnt(7)
	v_add_u32_e32 v76, 8192, v0
	v_cmp_gt_i32_e32 vcc, s33, v76
	v_lshrrev_b32_e32 v76, 25, v18
	v_bfe_u32 v77, v18, 13, 12
	v_min_u32_e32 v77, 31, v77
	v_xor_b32_e32 v77, s8, v77
	v_lshl_or_b32 v76, v76, 5, v77
	v_lshl_add_u32 v58, v76, 2, s6
	s_and_saveexec_b64 s[4:5], vcc
	ds_add_rtn_u32 v42, v58, v79
	s_or_b64 exec, exec, s[4:5]
	s_waitcnt vmcnt(6)
	v_add_u32_e32 v76, 9216, v0
	v_cmp_gt_i32_e32 vcc, s33, v76
	v_lshrrev_b32_e32 v76, 25, v20
	v_bfe_u32 v77, v20, 13, 12
	v_min_u32_e32 v77, 31, v77
	v_xor_b32_e32 v77, s8, v77
	v_lshl_or_b32 v76, v76, 5, v77
	v_lshl_add_u32 v59, v76, 2, s6
	s_and_saveexec_b64 s[4:5], vcc
	ds_add_rtn_u32 v43, v59, v79
	s_or_b64 exec, exec, s[4:5]
	s_waitcnt vmcnt(5)
	v_add_u32_e32 v76, 10240, v0
	v_cmp_gt_i32_e32 vcc, s33, v76
	v_lshrrev_b32_e32 v76, 25, v22
	v_bfe_u32 v77, v22, 13, 12
	v_min_u32_e32 v77, 31, v77
	v_xor_b32_e32 v77, s8, v77
	v_lshl_or_b32 v76, v76, 5, v77
	v_lshl_add_u32 v60, v76, 2, s6
	s_and_saveexec_b64 s[4:5], vcc
	ds_add_rtn_u32 v44, v60, v79
	s_or_b64 exec, exec, s[4:5]
	s_waitcnt vmcnt(4)
	v_add_u32_e32 v76, 11264, v0
	v_cmp_gt_i32_e32 vcc, s33, v76
	v_lshrrev_b32_e32 v76, 25, v24
	v_bfe_u32 v77, v24, 13, 12
	v_min_u32_e32 v77, 31, v77
	v_xor_b32_e32 v77, s8, v77
	v_lshl_or_b32 v76, v76, 5, v77
	v_lshl_add_u32 v61, v76, 2, s6
	s_and_saveexec_b64 s[4:5], vcc
	ds_add_rtn_u32 v45, v61, v79
	s_or_b64 exec, exec, s[4:5]
	s_waitcnt vmcnt(3)
	v_add_u32_e32 v76, 12288, v0
	v_cmp_gt_i32_e32 vcc, s33, v76
	v_lshrrev_b32_e32 v76, 25, v26
	v_bfe_u32 v77, v26, 13, 12
	v_min_u32_e32 v77, 31, v77
	v_xor_b32_e32 v77, s8, v77
	v_lshl_or_b32 v76, v76, 5, v77
	v_lshl_add_u32 v62, v76, 2, s6
	s_and_saveexec_b64 s[4:5], vcc
	ds_add_rtn_u32 v46, v62, v79
	s_or_b64 exec, exec, s[4:5]
	s_waitcnt vmcnt(2)
	v_add_u32_e32 v76, 13312, v0
	v_cmp_gt_i32_e32 vcc, s33, v76
	v_lshrrev_b32_e32 v76, 25, v28
	v_bfe_u32 v77, v28, 13, 12
	v_min_u32_e32 v77, 31, v77
	v_xor_b32_e32 v77, s8, v77
	v_lshl_or_b32 v76, v76, 5, v77
	v_lshl_add_u32 v63, v76, 2, s6
	s_and_saveexec_b64 s[4:5], vcc
	ds_add_rtn_u32 v47, v63, v79
	s_or_b64 exec, exec, s[4:5]
	s_waitcnt vmcnt(1)
	v_add_u32_e32 v76, 14336, v0
	v_cmp_gt_i32_e32 vcc, s33, v76
	v_lshrrev_b32_e32 v76, 25, v30
	v_bfe_u32 v77, v30, 13, 12
	v_min_u32_e32 v77, 31, v77
	v_xor_b32_e32 v77, s8, v77
	v_lshl_or_b32 v76, v76, 5, v77
	v_lshl_add_u32 v64, v76, 2, s6
	s_and_saveexec_b64 s[4:5], vcc
	ds_add_rtn_u32 v48, v64, v79
	s_or_b64 exec, exec, s[4:5]
	s_waitcnt vmcnt(0)
	v_add_u32_e32 v76, 15360, v0
	v_cmp_gt_i32_e32 vcc, s33, v76
	v_lshrrev_b32_e32 v76, 25, v32
	v_bfe_u32 v77, v32, 13, 12
	v_min_u32_e32 v77, 31, v77
	v_xor_b32_e32 v77, s8, v77
	v_lshl_or_b32 v76, v76, 5, v77
	v_lshl_add_u32 v65, v76, 2, s6
	s_and_saveexec_b64 s[4:5], vcc
	ds_add_rtn_u32 v49, v65, v79
	s_or_b64 exec, exec, s[4:5]
	s_waitcnt lgkmcnt(0)
	s_barrier
	ds_read_b128 v[66:69], v1
	v_mbcnt_lo_u32_b32 v70, -1, 0
	v_mbcnt_hi_u32_b32 v70, -1, v70
	v_lshrrev_b32_e32 v71, 6, v0
	s_waitcnt lgkmcnt(0)
	v_add_u32_e32 v74, v66, v67
	v_add_u32_e32 v75, v74, v68
	v_add_u32_e32 v73, v75, v69
	v_mov_b32_e32 v72, v73
	v_subrev_u32_e32 v77, 1, v70
	v_lshlrev_b32_e32 v77, 2, v77
	ds_bpermute_b32 v76, v77, v72
	v_cmp_le_u32_e32 vcc, 1, v70
	s_waitcnt lgkmcnt(0)
	v_cndmask_b32_e32 v76, 0, v76, vcc
	v_add_u32_e32 v72, v72, v76
	v_subrev_u32_e32 v77, 2, v70
	v_lshlrev_b32_e32 v77, 2, v77
	ds_bpermute_b32 v76, v77, v72
	v_cmp_le_u32_e32 vcc, 2, v70
	s_waitcnt lgkmcnt(0)
	v_cndmask_b32_e32 v76, 0, v76, vcc
	v_add_u32_e32 v72, v72, v76
	v_subrev_u32_e32 v77, 4, v70
	v_lshlrev_b32_e32 v77, 2, v77
	ds_bpermute_b32 v76, v77, v72
	v_cmp_le_u32_e32 vcc, 4, v70
	s_waitcnt lgkmcnt(0)
	v_cndmask_b32_e32 v76, 0, v76, vcc
	v_add_u32_e32 v72, v72, v76
	v_subrev_u32_e32 v77, 8, v70
	v_lshlrev_b32_e32 v77, 2, v77
	ds_bpermute_b32 v76, v77, v72
	v_cmp_le_u32_e32 vcc, 8, v70
	s_waitcnt lgkmcnt(0)
	v_cndmask_b32_e32 v76, 0, v76, vcc
	v_add_u32_e32 v72, v72, v76
	v_subrev_u32_e32 v77, 16, v70
	v_lshlrev_b32_e32 v77, 2, v77
	ds_bpermute_b32 v76, v77, v72
	v_cmp_le_u32_e32 vcc, 16, v70
	s_waitcnt lgkmcnt(0)
	v_cndmask_b32_e32 v76, 0, v76, vcc
	v_add_u32_e32 v72, v72, v76
	v_subrev_u32_e32 v77, 32, v70
	v_lshlrev_b32_e32 v77, 2, v77
	ds_bpermute_b32 v76, v77, v72
	v_cmp_le_u32_e32 vcc, 32, v70
	s_waitcnt lgkmcnt(0)
	v_cndmask_b32_e32 v76, 0, v76, vcc
	v_add_u32_e32 v72, v72, v76
	s_mov_b32 s7, 0x24000
	v_lshl_add_u32 v77, v71, 2, s7
	v_cmp_eq_u32_e32 vcc, 63, v70
	s_and_saveexec_b64 s[4:5], vcc
	ds_write_b32 v77, v72
	s_or_b64 exec, exec, s[4:5]
	s_waitcnt lgkmcnt(0)
	s_barrier
	v_mov_b32_e32 v77, s7
	ds_read_b128 v[80:83], v77
	ds_read_b128 v[84:87], v77 offset:16
	ds_read_b128 v[88:91], v77 offset:32
	ds_read_b128 v[92:95], v77 offset:48
	v_mov_b32_e32 v78, 0
	s_waitcnt lgkmcnt(0)
	v_cmp_lt_u32_e32 vcc, 0, v71
	v_cndmask_b32_e32 v76, 0, v80, vcc
	v_add_u32_e32 v78, v78, v76
	v_cmp_lt_u32_e32 vcc, 1, v71
	v_cndmask_b32_e32 v76, 0, v81, vcc
	v_add_u32_e32 v78, v78, v76
	v_cmp_lt_u32_e32 vcc, 2, v71
	v_cndmask_b32_e32 v76, 0, v82, vcc
	v_add_u32_e32 v78, v78, v76
	v_cmp_lt_u32_e32 vcc, 3, v71
	v_cndmask_b32_e32 v76, 0, v83, vcc
	v_add_u32_e32 v78, v78, v76
	v_cmp_lt_u32_e32 vcc, 4, v71
	v_cndmask_b32_e32 v76, 0, v84, vcc
	v_add_u32_e32 v78, v78, v76
	v_cmp_lt_u32_e32 vcc, 5, v71
	v_cndmask_b32_e32 v76, 0, v85, vcc
	v_add_u32_e32 v78, v78, v76
	v_cmp_lt_u32_e32 vcc, 6, v71
	v_cndmask_b32_e32 v76, 0, v86, vcc
	v_add_u32_e32 v78, v78, v76
	v_cmp_lt_u32_e32 vcc, 7, v71
	v_cndmask_b32_e32 v76, 0, v87, vcc
	v_add_u32_e32 v78, v78, v76
	v_cmp_lt_u32_e32 vcc, 8, v71
	v_cndmask_b32_e32 v76, 0, v88, vcc
	v_add_u32_e32 v78, v78, v76
	v_cmp_lt_u32_e32 vcc, 9, v71
	v_cndmask_b32_e32 v76, 0, v89, vcc
	v_add_u32_e32 v78, v78, v76
	v_cmp_lt_u32_e32 vcc, 10, v71
	v_cndmask_b32_e32 v76, 0, v90, vcc
	v_add_u32_e32 v78, v78, v76
	v_cmp_lt_u32_e32 vcc, 11, v71
	v_cndmask_b32_e32 v76, 0, v91, vcc
	v_add_u32_e32 v78, v78, v76
	v_cmp_lt_u32_e32 vcc, 12, v71
	v_cndmask_b32_e32 v76, 0, v92, vcc
	v_add_u32_e32 v78, v78, v76
	v_cmp_lt_u32_e32 vcc, 13, v71
	v_cndmask_b32_e32 v76, 0, v93, vcc
	v_add_u32_e32 v78, v78, v76
	v_cmp_lt_u32_e32 vcc, 14, v71
	v_cndmask_b32_e32 v76, 0, v94, vcc
	v_add_u32_e32 v78, v78, v76
	v_sub_u32_e32 v72, v72, v73
	v_add_u32_e32 v72, v72, v78
	v_add_u32_e32 v76, v72, v66
	v_add_u32_e32 v77, v72, v74
	v_add_u32_e32 v78, v72, v75
	v_mov_b32_e32 v66, v72
	v_mov_b32_e32 v67, v76
	v_mov_b32_e32 v68, v77
	v_mov_b32_e32 v69, v78
	ds_write_b128 v1, v[66:69]
	v_and_b32_e32 v76, 7, v0
	v_lshrrev_b32_e32 v77, 3, v0
	v_lshl_add_u32 v77, s42, 7, v77
	v_cmp_eq_u32_e32 vcc, 0, v76
	v_cmp_gt_i32_e64 s[4:5], s44, v77
	s_and_b64 s[4:5], vcc, s[4:5]
	v_add_u32_e32 v78, s36, v72
	v_lshlrev_b32_e32 v76, 2, v77
	s_and_saveexec_b64 s[8:9], s[4:5]
	global_store_dword v76, v78, s[38:39]
	s_add_i32 s7, s44, -1
	v_cmp_eq_u32_e32 vcc, s7, v77
	s_and_b64 exec, exec, vcc
	v_mov_b32_e32 v78, s45
	global_store_dword v76, v78, s[38:39] offset:4
	s_mov_b64 exec, s[8:9]
	s_waitcnt lgkmcnt(0)
	s_barrier
	v_add_u32_e32 v76, 0, v0
	v_cmp_gt_i32_e32 vcc, s33, v76
	s_and_saveexec_b64 s[4:5], vcc
	ds_read_b32 v50, v50
	s_or_b64 exec, exec, s[4:5]
	v_add_u32_e32 v76, 1024, v0
	v_cmp_gt_i32_e32 vcc, s33, v76
	s_and_saveexec_b64 s[4:5], vcc
	ds_read_b32 v51, v51
	s_or_b64 exec, exec, s[4:5]
	v_add_u32_e32 v76, 2048, v0
	v_cmp_gt_i32_e32 vcc, s33, v76
	s_and_saveexec_b64 s[4:5], vcc
	ds_read_b32 v52, v52
	s_or_b64 exec, exec, s[4:5]
	v_add_u32_e32 v76, 3072, v0
	v_cmp_gt_i32_e32 vcc, s33, v76
	s_and_saveexec_b64 s[4:5], vcc
	ds_read_b32 v53, v53
	s_or_b64 exec, exec, s[4:5]
	v_add_u32_e32 v76, 4096, v0
	v_cmp_gt_i32_e32 vcc, s33, v76
	s_and_saveexec_b64 s[4:5], vcc
	ds_read_b32 v54, v54
	s_or_b64 exec, exec, s[4:5]
	v_add_u32_e32 v76, 5120, v0
	v_cmp_gt_i32_e32 vcc, s33, v76
	s_and_saveexec_b64 s[4:5], vcc
	ds_read_b32 v55, v55
	s_or_b64 exec, exec, s[4:5]
	v_add_u32_e32 v76, 6144, v0
	v_cmp_gt_i32_e32 vcc, s33, v76
	s_and_saveexec_b64 s[4:5], vcc
	ds_read_b32 v56, v56
	s_or_b64 exec, exec, s[4:5]
	v_add_u32_e32 v76, 7168, v0
	v_cmp_gt_i32_e32 vcc, s33, v76
	s_and_saveexec_b64 s[4:5], vcc
	ds_read_b32 v57, v57
	s_or_b64 exec, exec, s[4:5]
	v_add_u32_e32 v76, 8192, v0
	v_cmp_gt_i32_e32 vcc, s33, v76
	s_and_saveexec_b64 s[4:5], vcc
	ds_read_b32 v58, v58
	s_or_b64 exec, exec, s[4:5]
	v_add_u32_e32 v76, 9216, v0
	v_cmp_gt_i32_e32 vcc, s33, v76
	s_and_saveexec_b64 s[4:5], vcc
	ds_read_b32 v59, v59
	s_or_b64 exec, exec, s[4:5]
	v_add_u32_e32 v76, 10240, v0
	v_cmp_gt_i32_e32 vcc, s33, v76
	s_and_saveexec_b64 s[4:5], vcc
	ds_read_b32 v60, v60
	s_or_b64 exec, exec, s[4:5]
	v_add_u32_e32 v76, 11264, v0
	v_cmp_gt_i32_e32 vcc, s33, v76
	s_and_saveexec_b64 s[4:5], vcc
	ds_read_b32 v61, v61
	s_or_b64 exec, exec, s[4:5]
	v_add_u32_e32 v76, 12288, v0
	v_cmp_gt_i32_e32 vcc, s33, v76
	s_and_saveexec_b64 s[4:5], vcc
	ds_read_b32 v62, v62
	s_or_b64 exec, exec, s[4:5]
	v_add_u32_e32 v76, 13312, v0
	v_cmp_gt_i32_e32 vcc, s33, v76
	s_and_saveexec_b64 s[4:5], vcc
	ds_read_b32 v63, v63
	s_or_b64 exec, exec, s[4:5]
	v_add_u32_e32 v76, 14336, v0
	v_cmp_gt_i32_e32 vcc, s33, v76
	s_and_saveexec_b64 s[4:5], vcc
	ds_read_b32 v64, v64
	s_or_b64 exec, exec, s[4:5]
	v_add_u32_e32 v76, 15360, v0
	v_cmp_gt_i32_e32 vcc, s33, v76
	s_and_saveexec_b64 s[4:5], vcc
	ds_read_b32 v65, v65
	s_or_b64 exec, exec, s[4:5]
	s_waitcnt lgkmcnt(0)
	s_barrier
	v_add_u32_e32 v76, 0, v0
	v_cmp_gt_i32_e32 vcc, s33, v76
	v_add_u32_e32 v77, v50, v34
	v_lshlrev_b32_e32 v77, 3, v77
	v_and_b32_e32 v2, 0x1ffffff, v2
	s_and_saveexec_b64 s[4:5], vcc
	ds_write_b64 v77, v[2:3]
	s_or_b64 exec, exec, s[4:5]
	v_add_u32_e32 v76, 1024, v0
	v_cmp_gt_i32_e32 vcc, s33, v76
	v_add_u32_e32 v77, v51, v35
	v_lshlrev_b32_e32 v77, 3, v77
	v_and_b32_e32 v4, 0x1ffffff, v4
	s_and_saveexec_b64 s[4:5], vcc
	ds_write_b64 v77, v[4:5]
	s_or_b64 exec, exec, s[4:5]
	v_add_u32_e32 v76, 2048, v0
	v_cmp_gt_i32_e32 vcc, s33, v76
	v_add_u32_e32 v77, v52, v36
	v_lshlrev_b32_e32 v77, 3, v77
	v_and_b32_e32 v6, 0x1ffffff, v6
	s_and_saveexec_b64 s[4:5], vcc
	ds_write_b64 v77, v[6:7]
	s_or_b64 exec, exec, s[4:5]
	v_add_u32_e32 v76, 3072, v0
	v_cmp_gt_i32_e32 vcc, s33, v76
	v_add_u32_e32 v77, v53, v37
	v_lshlrev_b32_e32 v77, 3, v77
	v_and_b32_e32 v8, 0x1ffffff, v8
	s_and_saveexec_b64 s[4:5], vcc
	ds_write_b64 v77, v[8:9]
	s_or_b64 exec, exec, s[4:5]
	v_add_u32_e32 v76, 4096, v0
	v_cmp_gt_i32_e32 vcc, s33, v76
	v_add_u32_e32 v77, v54, v38
	v_lshlrev_b32_e32 v77, 3, v77
	v_and_b32_e32 v10, 0x1ffffff, v10
	s_and_saveexec_b64 s[4:5], vcc
	ds_write_b64 v77, v[10:11]
	s_or_b64 exec, exec, s[4:5]
	v_add_u32_e32 v76, 5120, v0
	v_cmp_gt_i32_e32 vcc, s33, v76
	v_add_u32_e32 v77, v55, v39
	v_lshlrev_b32_e32 v77, 3, v77
	v_and_b32_e32 v12, 0x1ffffff, v12
	s_and_saveexec_b64 s[4:5], vcc
	ds_write_b64 v77, v[12:13]
	s_or_b64 exec, exec, s[4:5]
	v_add_u32_e32 v76, 6144, v0
	v_cmp_gt_i32_e32 vcc, s33, v76
	v_add_u32_e32 v77, v56, v40
	v_lshlrev_b32_e32 v77, 3, v77
	v_and_b32_e32 v14, 0x1ffffff, v14
	s_and_saveexec_b64 s[4:5], vcc
	ds_write_b64 v77, v[14:15]
	s_or_b64 exec, exec, s[4:5]
	v_add_u32_e32 v76, 7168, v0
	v_cmp_gt_i32_e32 vcc, s33, v76
	v_add_u32_e32 v77, v57, v41
	v_lshlrev_b32_e32 v77, 3, v77
	v_and_b32_e32 v16, 0x1ffffff, v16
	s_and_saveexec_b64 s[4:5], vcc
	ds_write_b64 v77, v[16:17]
	s_or_b64 exec, exec, s[4:5]
	v_add_u32_e32 v76, 8192, v0
	v_cmp_gt_i32_e32 vcc, s33, v76
	v_add_u32_e32 v77, v58, v42
	v_lshlrev_b32_e32 v77, 3, v77
	v_and_b32_e32 v18, 0x1ffffff, v18
	s_and_saveexec_b64 s[4:5], vcc
	ds_write_b64 v77, v[18:19]
	s_or_b64 exec, exec, s[4:5]
	v_add_u32_e32 v76, 9216, v0
	v_cmp_gt_i32_e32 vcc, s33, v76
	v_add_u32_e32 v77, v59, v43
	v_lshlrev_b32_e32 v77, 3, v77
	v_and_b32_e32 v20, 0x1ffffff, v20
	s_and_saveexec_b64 s[4:5], vcc
	ds_write_b64 v77, v[20:21]
	s_or_b64 exec, exec, s[4:5]
	v_add_u32_e32 v76, 10240, v0
	v_cmp_gt_i32_e32 vcc, s33, v76
	v_add_u32_e32 v77, v60, v44
	v_lshlrev_b32_e32 v77, 3, v77
	v_and_b32_e32 v22, 0x1ffffff, v22
	s_and_saveexec_b64 s[4:5], vcc
	ds_write_b64 v77, v[22:23]
	s_or_b64 exec, exec, s[4:5]
	v_add_u32_e32 v76, 11264, v0
	v_cmp_gt_i32_e32 vcc, s33, v76
	v_add_u32_e32 v77, v61, v45
	v_lshlrev_b32_e32 v77, 3, v77
	v_and_b32_e32 v24, 0x1ffffff, v24
	s_and_saveexec_b64 s[4:5], vcc
	ds_write_b64 v77, v[24:25]
	s_or_b64 exec, exec, s[4:5]
	v_add_u32_e32 v76, 12288, v0
	v_cmp_gt_i32_e32 vcc, s33, v76
	v_add_u32_e32 v77, v62, v46
	v_lshlrev_b32_e32 v77, 3, v77
	v_and_b32_e32 v26, 0x1ffffff, v26
	s_and_saveexec_b64 s[4:5], vcc
	ds_write_b64 v77, v[26:27]
	s_or_b64 exec, exec, s[4:5]
	v_add_u32_e32 v76, 13312, v0
	v_cmp_gt_i32_e32 vcc, s33, v76
	v_add_u32_e32 v77, v63, v47
	v_lshlrev_b32_e32 v77, 3, v77
	v_and_b32_e32 v28, 0x1ffffff, v28
	s_and_saveexec_b64 s[4:5], vcc
	ds_write_b64 v77, v[28:29]
	s_or_b64 exec, exec, s[4:5]
	v_add_u32_e32 v76, 14336, v0
	v_cmp_gt_i32_e32 vcc, s33, v76
	v_add_u32_e32 v77, v64, v48
	v_lshlrev_b32_e32 v77, 3, v77
	v_and_b32_e32 v30, 0x1ffffff, v30
	s_and_saveexec_b64 s[4:5], vcc
	ds_write_b64 v77, v[30:31]
	s_or_b64 exec, exec, s[4:5]
	v_add_u32_e32 v76, 15360, v0
	v_cmp_gt_i32_e32 vcc, s33, v76
	v_add_u32_e32 v77, v65, v49
	v_lshlrev_b32_e32 v77, 3, v77
	v_and_b32_e32 v32, 0x1ffffff, v32
	s_and_saveexec_b64 s[4:5], vcc
	ds_write_b64 v77, v[32:33]
	s_or_b64 exec, exec, s[4:5]
	s_waitcnt lgkmcnt(0)
	s_barrier
	v_cmp_gt_i32_e32 vcc, s33, v0
	s_and_saveexec_b64 s[0:1], vcc
	s_cbranch_execz .LBB3_141
	v_add_u32_e32 v2, s36, v0
	v_ashrrev_i32_e32 v3, 31, v2
	v_lshl_add_u64 v[2:3], v[2:3], 3, s[40:41]
	v_lshlrev_b32_e32 v1, 3, v0
	s_mov_b64 s[0:1], 0
	s_mov_b64 s[2:3], 0x2000

_Z6k_spmmILb0ELi0EEvPKiPK15HIP_vector_typeIiLj2EEPKvPKfPKDF16_S9_S9_iPfPDF16_PhSC_PKhS9_SG_S9_S9_i:
	s_load_dword s3, s[0:1], 0x90
	s_load_dwordx2 s[6:7], s[0:1], 0x8
	s_load_dword s4, s[0:1], 0x38
	v_lshrrev_b32_e32 v1, 4, v0
	s_waitcnt lgkmcnt(0)
	s_lshr_b32 s13, s3, 12
	s_lshl_b32 s13, s13, 12
	s_cmp_lt_u32 s2, s13
	s_cbranch_scc0 .Lperm_skip0
	s_and_b32 s14, s2, 511
	s_lshr_b32 s15, s2, 9
	s_lshr_b32 s16, s15, 2
	s_and_b32 s17, s15, 1
	s_bfe_u32 s15, s15, 0x10001
	s_lshl_b32 s16, s16, 1
	s_add_i32 s16, s16, s17
	s_lshl_b32 s16, s16, 10
	s_lshl_b32 s15, s15, 9
	s_or_b32 s2, s16, s15
	s_or_b32 s2, s2, s14
.Lperm_skip0:
	s_not_b32 s2, s2
	s_add_i32 s12, s3, s2
	v_bfe_u32 v2, v0, 4, 2
	s_lshl_b32 s2, s12, 5
	v_and_b32_e32 v3, 28, v1
	v_or3_b32 v98, s2, v3, v2
	v_cmp_gt_i32_e64 s[2:3], s4, v98
	v_mov_b32_e32 v2, 0
	v_ashrrev_i32_e32 v99, 31, v98
	v_mov_b32_e32 v101, 0
	v_mov_b32_e32 v4, 0
	s_and_saveexec_b64 s[4:5], s[2:3]
	s_cbranch_execz .LBB4_2
	s_load_dwordx2 s[8:9], s[0:1], 0x0
	s_waitcnt lgkmcnt(0)
	v_lshl_add_u64 v[4:5], v[98:99], 2, s[8:9]
	global_load_dwordx2 v[4:5], v[4:5], off
	s_waitcnt vmcnt(0)
	v_sub_u32_e32 v101, v5, v4
